# speedup vs baseline: 1.0102x; 1.0000x over previous
.LBB0_2:
	s_add_i32 s12, s4, 0xffffb000
	s_and_b32 s12, s12, 0x1e000
	s_lshl_b32 s12, s12, 4
	s_waitcnt lgkmcnt(0)
	s_barrier
	v_lshl_add_u64 v[166:167], v[130:131], 0, s[12:13]
	global_load_dwordx4 v[134:137], v[166:167], off
	global_load_dwordx4 v[138:141], v[166:167], off offset:1024
	global_load_dwordx4 v[142:145], v[166:167], off offset:2048
	global_load_dwordx4 v[146:149], v[166:167], off offset:3072
	ds_read_b128 v[150:153], v132
	ds_read_b128 v[154:157], v132 offset:2048
	ds_read_b128 v[158:161], v132 offset:4096
	ds_read_b128 v[162:165], v132 offset:6144
	s_setprio 2
	s_waitcnt vmcnt(19) lgkmcnt(3)
	v_mfma_f32_16x16x32_f16 v[50:53], v[54:57], v[150:153], v[50:53]
	s_waitcnt vmcnt(18)
	v_mfma_f32_16x16x32_f16 v[70:73], v[58:61], v[150:153], v[70:73]
	s_waitcnt vmcnt(17)
	v_mfma_f32_16x16x32_f16 v[74:77], v[62:65], v[150:153], v[74:77]
	s_waitcnt vmcnt(16)
	v_mfma_f32_16x16x32_f16 v[78:81], v[66:69], v[150:153], v[78:81]
	s_waitcnt lgkmcnt(2)
	v_mfma_f32_16x16x32_f16 v[82:85], v[54:57], v[154:157], v[82:85]
	v_mfma_f32_16x16x32_f16 v[86:89], v[58:61], v[154:157], v[86:89]
	v_mfma_f32_16x16x32_f16 v[90:93], v[62:65], v[154:157], v[90:93]
	v_mfma_f32_16x16x32_f16 v[94:97], v[66:69], v[154:157], v[94:97]
	s_waitcnt lgkmcnt(1)
	v_mfma_f32_16x16x32_f16 v[98:101], v[54:57], v[158:161], v[98:101]
	v_mfma_f32_16x16x32_f16 v[102:105], v[58:61], v[158:161], v[102:105]
	v_mfma_f32_16x16x32_f16 v[106:109], v[62:65], v[158:161], v[106:109]
	v_mfma_f32_16x16x32_f16 v[110:113], v[66:69], v[158:161], v[110:113]
	s_waitcnt lgkmcnt(0)
	v_mfma_f32_16x16x32_f16 v[54:57], v[54:57], v[162:165], v[114:117]
	v_mfma_f32_16x16x32_f16 v[58:61], v[58:61], v[162:165], v[118:121]
	v_mfma_f32_16x16x32_f16 v[62:65], v[62:65], v[162:165], v[122:125]
	v_mfma_f32_16x16x32_f16 v[66:69], v[66:69], v[162:165], v[126:129]
	s_setprio 1
	s_nop 1
	v_add_co_u32_e32 v126, vcc, s3, v166
	s_nop 1
	v_addc_co_u32_e32 v127, vcc, 0, v167, vcc
	global_load_dwordx4 v[114:117], v[126:127], off
	global_load_dwordx4 v[118:121], v[126:127], off offset:1024
	global_load_dwordx4 v[122:125], v[126:127], off offset:2048
	s_nop 0
	global_load_dwordx4 v[126:129], v[126:127], off offset:3072
	ds_read_b128 v[150:153], v132 offset:1024
	ds_read_b128 v[154:157], v132 offset:3072
	ds_read_b128 v[158:161], v132 offset:5120
	ds_read_b128 v[162:165], v132 offset:7168
	s_setprio 2
	s_waitcnt vmcnt(19) lgkmcnt(3)
	v_mfma_f32_16x16x32_f16 v[50:53], v[34:37], v[150:153], v[50:53]
	s_waitcnt vmcnt(18)
	v_mfma_f32_16x16x32_f16 v[70:73], v[38:41], v[150:153], v[70:73]
	s_waitcnt vmcnt(17)
	v_mfma_f32_16x16x32_f16 v[74:77], v[42:45], v[150:153], v[74:77]
	s_waitcnt vmcnt(16)
	v_mfma_f32_16x16x32_f16 v[78:81], v[46:49], v[150:153], v[78:81]
	s_waitcnt lgkmcnt(2)
	v_mfma_f32_16x16x32_f16 v[82:85], v[34:37], v[154:157], v[82:85]
	v_mfma_f32_16x16x32_f16 v[86:89], v[38:41], v[154:157], v[86:89]
	v_mfma_f32_16x16x32_f16 v[90:93], v[42:45], v[154:157], v[90:93]
	v_mfma_f32_16x16x32_f16 v[94:97], v[46:49], v[154:157], v[94:97]
	s_waitcnt lgkmcnt(1)
	v_mfma_f32_16x16x32_f16 v[98:101], v[34:37], v[158:161], v[98:101]
	v_mfma_f32_16x16x32_f16 v[102:105], v[38:41], v[158:161], v[102:105]
	v_mfma_f32_16x16x32_f16 v[106:109], v[42:45], v[158:161], v[106:109]
	v_mfma_f32_16x16x32_f16 v[110:113], v[46:49], v[158:161], v[110:113]
	s_waitcnt lgkmcnt(0)
	v_mfma_f32_16x16x32_f16 v[34:37], v[34:37], v[162:165], v[54:57]
	v_mfma_f32_16x16x32_f16 v[38:41], v[38:41], v[162:165], v[58:61]
	v_mfma_f32_16x16x32_f16 v[42:45], v[42:45], v[162:165], v[62:65]
	v_mfma_f32_16x16x32_f16 v[46:49], v[46:49], v[162:165], v[66:69]
	s_setprio 1
	s_add_i32 s12, s4, 0xffffc000
	s_and_b32 s12, s12, 0x1f000
	s_lshl_b32 s12, s12, 4
	s_waitcnt lgkmcnt(0)
	s_barrier
	v_lshl_add_u64 v[166:167], v[130:131], 0, s[12:13]
	global_load_dwordx4 v[54:57], v[166:167], off
	global_load_dwordx4 v[58:61], v[166:167], off offset:1024
	global_load_dwordx4 v[62:65], v[166:167], off offset:2048
	global_load_dwordx4 v[66:69], v[166:167], off offset:3072
	ds_read_b128 v[150:153], v132 offset:8192
	ds_read_b128 v[154:157], v132 offset:10240
	ds_read_b128 v[158:161], v132 offset:12288
	ds_read_b128 v[162:165], v132 offset:14336
	s_setprio 2
	s_waitcnt vmcnt(16) lgkmcnt(3)
	v_mfma_f32_16x16x32_f16 v[50:53], v[30:33], v[150:153], v[50:53]
	v_mfma_f32_16x16x32_f16 v[70:73], v[18:21], v[150:153], v[70:73]
	v_mfma_f32_16x16x32_f16 v[74:77], v[22:25], v[150:153], v[74:77]
	v_mfma_f32_16x16x32_f16 v[78:81], v[26:29], v[150:153], v[78:81]
	s_waitcnt lgkmcnt(2)
	v_mfma_f32_16x16x32_f16 v[82:85], v[30:33], v[154:157], v[82:85]
	v_mfma_f32_16x16x32_f16 v[86:89], v[18:21], v[154:157], v[86:89]
	v_mfma_f32_16x16x32_f16 v[90:93], v[22:25], v[154:157], v[90:93]
	v_mfma_f32_16x16x32_f16 v[94:97], v[26:29], v[154:157], v[94:97]
	s_waitcnt lgkmcnt(1)
	v_mfma_f32_16x16x32_f16 v[98:101], v[30:33], v[158:161], v[98:101]
	v_mfma_f32_16x16x32_f16 v[102:105], v[18:21], v[158:161], v[102:105]
	v_mfma_f32_16x16x32_f16 v[106:109], v[22:25], v[158:161], v[106:109]
	v_mfma_f32_16x16x32_f16 v[110:113], v[26:29], v[158:161], v[110:113]
	s_waitcnt lgkmcnt(0)
	v_mfma_f32_16x16x32_f16 v[30:33], v[30:33], v[162:165], v[34:37]
	v_mfma_f32_16x16x32_f16 v[18:21], v[18:21], v[162:165], v[38:41]
	v_mfma_f32_16x16x32_f16 v[22:25], v[22:25], v[162:165], v[42:45]
	v_mfma_f32_16x16x32_f16 v[26:29], v[26:29], v[162:165], v[46:49]
	s_setprio 1
	s_nop 1
	v_add_co_u32_e32 v46, vcc, s3, v166
	s_nop 1
	v_addc_co_u32_e32 v47, vcc, 0, v167, vcc
	global_load_dwordx4 v[34:37], v[46:47], off
	global_load_dwordx4 v[38:41], v[46:47], off offset:1024
	global_load_dwordx4 v[42:45], v[46:47], off offset:2048
	s_nop 0
	global_load_dwordx4 v[46:49], v[46:47], off offset:3072
	ds_read_b128 v[150:153], v132 offset:9216
	ds_read_b128 v[154:157], v132 offset:11264
	ds_read_b128 v[158:161], v132 offset:13312
	ds_read_b128 v[162:165], v132 offset:15360
	s_setprio 2
	s_waitcnt vmcnt(19) lgkmcnt(3)
	v_mfma_f32_16x16x32_f16 v[50:53], v[2:5], v[150:153], v[50:53]
	s_waitcnt vmcnt(18)
	v_mfma_f32_16x16x32_f16 v[70:73], v[6:9], v[150:153], v[70:73]
	s_waitcnt vmcnt(17)
	v_mfma_f32_16x16x32_f16 v[74:77], v[10:13], v[150:153], v[74:77]
	s_waitcnt vmcnt(16)
	v_mfma_f32_16x16x32_f16 v[78:81], v[14:17], v[150:153], v[78:81]
	s_waitcnt lgkmcnt(2)
	v_mfma_f32_16x16x32_f16 v[82:85], v[2:5], v[154:157], v[82:85]
	v_mfma_f32_16x16x32_f16 v[86:89], v[6:9], v[154:157], v[86:89]
	v_mfma_f32_16x16x32_f16 v[90:93], v[10:13], v[154:157], v[90:93]
	v_mfma_f32_16x16x32_f16 v[94:97], v[14:17], v[154:157], v[94:97]
	s_waitcnt lgkmcnt(1)
	v_mfma_f32_16x16x32_f16 v[98:101], v[2:5], v[158:161], v[98:101]
	v_mfma_f32_16x16x32_f16 v[102:105], v[6:9], v[158:161], v[102:105]
	v_mfma_f32_16x16x32_f16 v[106:109], v[10:13], v[158:161], v[106:109]
	v_mfma_f32_16x16x32_f16 v[110:113], v[14:17], v[158:161], v[110:113]
	s_waitcnt lgkmcnt(0)
	v_mfma_f32_16x16x32_f16 v[2:5], v[2:5], v[162:165], v[30:33]
	v_mfma_f32_16x16x32_f16 v[6:9], v[6:9], v[162:165], v[18:21]
	v_mfma_f32_16x16x32_f16 v[10:13], v[10:13], v[162:165], v[22:25]
	v_mfma_f32_16x16x32_f16 v[14:17], v[14:17], v[162:165], v[26:29]
	s_setprio 1
	s_add_i32 s12, s4, 0xffffd000
	s_and_b32 s12, s12, 0x1e000
	s_lshl_b32 s12, s12, 4
	s_waitcnt lgkmcnt(0)
	s_barrier
	v_lshl_add_u64 v[166:167], v[130:131], 0, s[12:13]
	global_load_dwordx4 v[18:21], v[166:167], off
	global_load_dwordx4 v[22:25], v[166:167], off offset:1024
	global_load_dwordx4 v[26:29], v[166:167], off offset:2048
	global_load_dwordx4 v[30:33], v[166:167], off offset:3072
	ds_read_b128 v[150:153], v132
	ds_read_b128 v[154:157], v132 offset:2048
	ds_read_b128 v[158:161], v132 offset:4096
	ds_read_b128 v[162:165], v132 offset:6144
	s_setprio 2
	s_waitcnt vmcnt(19) lgkmcnt(3)
	v_mfma_f32_16x16x32_f16 v[50:53], v[134:137], v[150:153], v[50:53]
	s_waitcnt vmcnt(18)
	v_mfma_f32_16x16x32_f16 v[70:73], v[138:141], v[150:153], v[70:73]
	s_waitcnt vmcnt(17)
	v_mfma_f32_16x16x32_f16 v[74:77], v[142:145], v[150:153], v[74:77]
	s_waitcnt vmcnt(16)
	v_mfma_f32_16x16x32_f16 v[78:81], v[146:149], v[150:153], v[78:81]
	s_waitcnt lgkmcnt(2)
	v_mfma_f32_16x16x32_f16 v[82:85], v[134:137], v[154:157], v[82:85]
	v_mfma_f32_16x16x32_f16 v[86:89], v[138:141], v[154:157], v[86:89]
	v_mfma_f32_16x16x32_f16 v[90:93], v[142:145], v[154:157], v[90:93]
	v_mfma_f32_16x16x32_f16 v[94:97], v[146:149], v[154:157], v[94:97]
	s_waitcnt lgkmcnt(1)
	v_mfma_f32_16x16x32_f16 v[98:101], v[134:137], v[158:161], v[98:101]
	v_mfma_f32_16x16x32_f16 v[102:105], v[138:141], v[158:161], v[102:105]
	v_mfma_f32_16x16x32_f16 v[106:109], v[142:145], v[158:161], v[106:109]
	v_mfma_f32_16x16x32_f16 v[110:113], v[146:149], v[158:161], v[110:113]
	s_waitcnt lgkmcnt(0)
	v_mfma_f32_16x16x32_f16 v[2:5], v[134:137], v[162:165], v[2:5]
	v_mfma_f32_16x16x32_f16 v[6:9], v[138:141], v[162:165], v[6:9]
	v_mfma_f32_16x16x32_f16 v[10:13], v[142:145], v[162:165], v[10:13]
	v_mfma_f32_16x16x32_f16 v[14:17], v[146:149], v[162:165], v[14:17]
	s_setprio 1
	v_add_co_u32_e32 v146, vcc, s3, v166
	s_nop 1
	v_addc_co_u32_e32 v147, vcc, 0, v167, vcc
	global_load_dwordx4 v[134:137], v[146:147], off
	global_load_dwordx4 v[138:141], v[146:147], off offset:1024
	global_load_dwordx4 v[142:145], v[146:147], off offset:2048
	s_nop 0
	global_load_dwordx4 v[146:149], v[146:147], off offset:3072
	ds_read_b128 v[150:153], v132 offset:1024
	ds_read_b128 v[154:157], v132 offset:3072
	ds_read_b128 v[158:161], v132 offset:5120
	ds_read_b128 v[162:165], v132 offset:7168
	s_setprio 2
	s_waitcnt vmcnt(19) lgkmcnt(3)
	v_mfma_f32_16x16x32_f16 v[50:53], v[114:117], v[150:153], v[50:53]
	s_waitcnt vmcnt(18)
	v_mfma_f32_16x16x32_f16 v[70:73], v[118:121], v[150:153], v[70:73]
	s_waitcnt vmcnt(17)
	v_mfma_f32_16x16x32_f16 v[74:77], v[122:125], v[150:153], v[74:77]
	s_waitcnt vmcnt(16)
	v_mfma_f32_16x16x32_f16 v[78:81], v[126:129], v[150:153], v[78:81]
	s_waitcnt lgkmcnt(2)
	v_mfma_f32_16x16x32_f16 v[82:85], v[114:117], v[154:157], v[82:85]
	v_mfma_f32_16x16x32_f16 v[86:89], v[118:121], v[154:157], v[86:89]
	v_mfma_f32_16x16x32_f16 v[90:93], v[122:125], v[154:157], v[90:93]
	v_mfma_f32_16x16x32_f16 v[94:97], v[126:129], v[154:157], v[94:97]
	s_waitcnt lgkmcnt(1)
	v_mfma_f32_16x16x32_f16 v[98:101], v[114:117], v[158:161], v[98:101]
	v_mfma_f32_16x16x32_f16 v[102:105], v[118:121], v[158:161], v[102:105]
	v_mfma_f32_16x16x32_f16 v[106:109], v[122:125], v[158:161], v[106:109]
	v_mfma_f32_16x16x32_f16 v[110:113], v[126:129], v[158:161], v[110:113]
	s_waitcnt lgkmcnt(0)
	v_mfma_f32_16x16x32_f16 v[2:5], v[114:117], v[162:165], v[2:5]
	v_mfma_f32_16x16x32_f16 v[6:9], v[118:121], v[162:165], v[6:9]
	v_mfma_f32_16x16x32_f16 v[10:13], v[122:125], v[162:165], v[10:13]
	v_mfma_f32_16x16x32_f16 v[14:17], v[126:129], v[162:165], v[14:17]
	s_setprio 1
	s_add_i32 s12, s4, 0xffffe000
	s_and_b32 s12, s12, 0x1f000
	s_lshl_b32 s12, s12, 4
	s_waitcnt lgkmcnt(0)
	s_barrier
	v_lshl_add_u64 v[166:167], v[130:131], 0, s[12:13]
	global_load_dwordx4 v[114:117], v[166:167], off
	global_load_dwordx4 v[118:121], v[166:167], off offset:1024
	global_load_dwordx4 v[122:125], v[166:167], off offset:2048
	global_load_dwordx4 v[126:129], v[166:167], off offset:3072
	ds_read_b128 v[150:153], v132 offset:8192
	ds_read_b128 v[154:157], v132 offset:10240
	ds_read_b128 v[158:161], v132 offset:12288
	ds_read_b128 v[162:165], v132 offset:14336
	s_setprio 2
	s_waitcnt vmcnt(19) lgkmcnt(3)
	v_mfma_f32_16x16x32_f16 v[50:53], v[54:57], v[150:153], v[50:53]
	s_waitcnt vmcnt(18)
	v_mfma_f32_16x16x32_f16 v[70:73], v[58:61], v[150:153], v[70:73]
	s_waitcnt vmcnt(17)
	v_mfma_f32_16x16x32_f16 v[74:77], v[62:65], v[150:153], v[74:77]
	s_waitcnt vmcnt(16)
	v_mfma_f32_16x16x32_f16 v[78:81], v[66:69], v[150:153], v[78:81]
	s_waitcnt lgkmcnt(2)
	v_mfma_f32_16x16x32_f16 v[82:85], v[54:57], v[154:157], v[82:85]
	v_mfma_f32_16x16x32_f16 v[86:89], v[58:61], v[154:157], v[86:89]
	v_mfma_f32_16x16x32_f16 v[90:93], v[62:65], v[154:157], v[90:93]
	v_mfma_f32_16x16x32_f16 v[94:97], v[66:69], v[154:157], v[94:97]
	s_waitcnt lgkmcnt(1)
	v_mfma_f32_16x16x32_f16 v[98:101], v[54:57], v[158:161], v[98:101]
	v_mfma_f32_16x16x32_f16 v[102:105], v[58:61], v[158:161], v[102:105]
	v_mfma_f32_16x16x32_f16 v[106:109], v[62:65], v[158:161], v[106:109]
	v_mfma_f32_16x16x32_f16 v[110:113], v[66:69], v[158:161], v[110:113]
	s_waitcnt lgkmcnt(0)
	v_mfma_f32_16x16x32_f16 v[2:5], v[54:57], v[162:165], v[2:5]
	v_mfma_f32_16x16x32_f16 v[6:9], v[58:61], v[162:165], v[6:9]
	v_mfma_f32_16x16x32_f16 v[10:13], v[62:65], v[162:165], v[10:13]
	v_mfma_f32_16x16x32_f16 v[14:17], v[66:69], v[162:165], v[14:17]
	s_setprio 1
	v_add_co_u32_e32 v54, vcc, s3, v166
	s_nop 1
	v_addc_co_u32_e32 v55, vcc, 0, v167, vcc
	global_load_dwordx4 v[150:153], v[54:55], off
	global_load_dwordx4 v[154:157], v[54:55], off offset:1024
	global_load_dwordx4 v[158:161], v[54:55], off offset:2048
	global_load_dwordx4 v[162:165], v[54:55], off offset:3072
	ds_read_b128 v[54:57], v132 offset:9216
	ds_read_b128 v[58:61], v132 offset:11264
	ds_read_b128 v[62:65], v132 offset:13312
	ds_read_b128 v[66:69], v132 offset:15360
	s_setprio 2
	s_waitcnt vmcnt(19) lgkmcnt(3)
	v_mfma_f32_16x16x32_f16 v[50:53], v[34:37], v[54:57], v[50:53]
	s_waitcnt vmcnt(18)
	v_mfma_f32_16x16x32_f16 v[70:73], v[38:41], v[54:57], v[70:73]
	s_waitcnt vmcnt(17)
	v_mfma_f32_16x16x32_f16 v[74:77], v[42:45], v[54:57], v[74:77]
	s_waitcnt vmcnt(16)
	v_mfma_f32_16x16x32_f16 v[78:81], v[46:49], v[54:57], v[78:81]
	s_waitcnt lgkmcnt(2)
	v_mfma_f32_16x16x32_f16 v[82:85], v[34:37], v[58:61], v[82:85]
	v_mfma_f32_16x16x32_f16 v[86:89], v[38:41], v[58:61], v[86:89]
	v_mfma_f32_16x16x32_f16 v[90:93], v[42:45], v[58:61], v[90:93]
	v_mfma_f32_16x16x32_f16 v[94:97], v[46:49], v[58:61], v[94:97]
	s_waitcnt lgkmcnt(1)
	v_mfma_f32_16x16x32_f16 v[98:101], v[34:37], v[62:65], v[98:101]
	v_mfma_f32_16x16x32_f16 v[102:105], v[38:41], v[62:65], v[102:105]
	v_mfma_f32_16x16x32_f16 v[106:109], v[42:45], v[62:65], v[106:109]
	v_mfma_f32_16x16x32_f16 v[110:113], v[46:49], v[62:65], v[110:113]
	s_waitcnt lgkmcnt(0)
	v_mfma_f32_16x16x32_f16 v[2:5], v[34:37], v[66:69], v[2:5]
	v_mfma_f32_16x16x32_f16 v[6:9], v[38:41], v[66:69], v[6:9]
	v_mfma_f32_16x16x32_f16 v[10:13], v[42:45], v[66:69], v[10:13]
	v_mfma_f32_16x16x32_f16 v[14:17], v[46:49], v[66:69], v[14:17]
	s_setprio 1
	s_add_i32 s12, s4, 0xfffff000
	s_and_b32 s12, s12, 0x1e000
	s_lshl_b32 s12, s12, 4
	s_waitcnt lgkmcnt(0)
	s_barrier
	v_lshl_add_u64 v[166:167], v[130:131], 0, s[12:13]
	global_load_dwordx4 v[54:57], v[166:167], off
	global_load_dwordx4 v[58:61], v[166:167], off offset:1024
	global_load_dwordx4 v[62:65], v[166:167], off offset:2048
	global_load_dwordx4 v[66:69], v[166:167], off offset:3072
	ds_read_b128 v[34:37], v132
	ds_read_b128 v[38:41], v132 offset:2048
	ds_read_b128 v[42:45], v132 offset:4096
	ds_read_b128 v[46:49], v132 offset:6144
	s_setprio 2
	s_waitcnt vmcnt(19) lgkmcnt(3)
	v_mfma_f32_16x16x32_f16 v[50:53], v[18:21], v[34:37], v[50:53]
	s_waitcnt vmcnt(18)
	v_mfma_f32_16x16x32_f16 v[70:73], v[22:25], v[34:37], v[70:73]
	s_waitcnt vmcnt(17)
	v_mfma_f32_16x16x32_f16 v[74:77], v[26:29], v[34:37], v[74:77]
	s_waitcnt vmcnt(16)
	v_mfma_f32_16x16x32_f16 v[78:81], v[30:33], v[34:37], v[78:81]
	s_waitcnt lgkmcnt(2)
	v_mfma_f32_16x16x32_f16 v[82:85], v[18:21], v[38:41], v[82:85]
	v_mfma_f32_16x16x32_f16 v[86:89], v[22:25], v[38:41], v[86:89]
	v_mfma_f32_16x16x32_f16 v[90:93], v[26:29], v[38:41], v[90:93]
	v_mfma_f32_16x16x32_f16 v[94:97], v[30:33], v[38:41], v[94:97]
	s_waitcnt lgkmcnt(1)
	v_mfma_f32_16x16x32_f16 v[98:101], v[18:21], v[42:45], v[98:101]
	v_mfma_f32_16x16x32_f16 v[102:105], v[22:25], v[42:45], v[102:105]
	v_mfma_f32_16x16x32_f16 v[106:109], v[26:29], v[42:45], v[106:109]
	v_mfma_f32_16x16x32_f16 v[110:113], v[30:33], v[42:45], v[110:113]
	s_waitcnt lgkmcnt(0)
	v_mfma_f32_16x16x32_f16 v[2:5], v[18:21], v[46:49], v[2:5]
	v_mfma_f32_16x16x32_f16 v[6:9], v[22:25], v[46:49], v[6:9]
	v_mfma_f32_16x16x32_f16 v[10:13], v[26:29], v[46:49], v[10:13]
	v_mfma_f32_16x16x32_f16 v[14:17], v[30:33], v[46:49], v[14:17]
	s_setprio 1
	v_add_co_u32_e32 v18, vcc, s3, v166
	s_nop 1
	v_addc_co_u32_e32 v19, vcc, 0, v167, vcc
	global_load_dwordx4 v[34:37], v[18:19], off
	global_load_dwordx4 v[38:41], v[18:19], off offset:1024
	global_load_dwordx4 v[42:45], v[18:19], off offset:2048
	global_load_dwordx4 v[46:49], v[18:19], off offset:3072
	ds_read_b128 v[18:21], v132 offset:1024
	ds_read_b128 v[22:25], v132 offset:3072
	ds_read_b128 v[26:29], v132 offset:5120
	ds_read_b128 v[30:33], v132 offset:7168
	s_setprio 2
	s_waitcnt vmcnt(19) lgkmcnt(3)
	v_mfma_f32_16x16x32_f16 v[50:53], v[134:137], v[18:21], v[50:53]
	s_waitcnt vmcnt(18)
	v_mfma_f32_16x16x32_f16 v[70:73], v[138:141], v[18:21], v[70:73]
	s_waitcnt vmcnt(17)
	v_mfma_f32_16x16x32_f16 v[74:77], v[142:145], v[18:21], v[74:77]
	s_waitcnt vmcnt(16)
	v_mfma_f32_16x16x32_f16 v[78:81], v[146:149], v[18:21], v[78:81]
	s_waitcnt lgkmcnt(2)
	v_mfma_f32_16x16x32_f16 v[82:85], v[134:137], v[22:25], v[82:85]
	v_mfma_f32_16x16x32_f16 v[86:89], v[138:141], v[22:25], v[86:89]
	v_mfma_f32_16x16x32_f16 v[90:93], v[142:145], v[22:25], v[90:93]
	v_mfma_f32_16x16x32_f16 v[94:97], v[146:149], v[22:25], v[94:97]
	s_waitcnt lgkmcnt(1)
	v_mfma_f32_16x16x32_f16 v[98:101], v[134:137], v[26:29], v[98:101]
	v_mfma_f32_16x16x32_f16 v[102:105], v[138:141], v[26:29], v[102:105]
	v_mfma_f32_16x16x32_f16 v[106:109], v[142:145], v[26:29], v[106:109]
	v_mfma_f32_16x16x32_f16 v[110:113], v[146:149], v[26:29], v[110:113]
	s_waitcnt lgkmcnt(0)
	v_mfma_f32_16x16x32_f16 v[2:5], v[134:137], v[30:33], v[2:5]
	v_mfma_f32_16x16x32_f16 v[6:9], v[138:141], v[30:33], v[6:9]
	v_mfma_f32_16x16x32_f16 v[10:13], v[142:145], v[30:33], v[10:13]
	v_mfma_f32_16x16x32_f16 v[14:17], v[146:149], v[30:33], v[14:17]
	s_setprio 1
	s_and_b32 s12, s4, 0x1f000
	s_lshl_b32 s12, s12, 4
	s_waitcnt lgkmcnt(0)
	s_barrier
	v_lshl_add_u64 v[166:167], v[130:131], 0, s[12:13]
	global_load_dwordx4 v[30:33], v[166:167], off
	global_load_dwordx4 v[18:21], v[166:167], off offset:1024
	global_load_dwordx4 v[22:25], v[166:167], off offset:2048
	global_load_dwordx4 v[26:29], v[166:167], off offset:3072
	ds_read_b128 v[134:137], v132 offset:8192
	ds_read_b128 v[138:141], v132 offset:10240
	ds_read_b128 v[142:145], v132 offset:12288
	ds_read_b128 v[146:149], v132 offset:14336
	s_setprio 2
	s_waitcnt vmcnt(19) lgkmcnt(3)
	v_mfma_f32_16x16x32_f16 v[50:53], v[114:117], v[134:137], v[50:53]
	s_waitcnt vmcnt(18)
	v_mfma_f32_16x16x32_f16 v[70:73], v[118:121], v[134:137], v[70:73]
	s_waitcnt vmcnt(17)
	v_mfma_f32_16x16x32_f16 v[74:77], v[122:125], v[134:137], v[74:77]
	s_waitcnt vmcnt(16)
	v_mfma_f32_16x16x32_f16 v[78:81], v[126:129], v[134:137], v[78:81]
	s_waitcnt lgkmcnt(2)
	v_mfma_f32_16x16x32_f16 v[82:85], v[114:117], v[138:141], v[82:85]
	v_mfma_f32_16x16x32_f16 v[86:89], v[118:121], v[138:141], v[86:89]
	v_mfma_f32_16x16x32_f16 v[90:93], v[122:125], v[138:141], v[90:93]
	v_mfma_f32_16x16x32_f16 v[94:97], v[126:129], v[138:141], v[94:97]
	s_waitcnt lgkmcnt(1)
	v_mfma_f32_16x16x32_f16 v[98:101], v[114:117], v[142:145], v[98:101]
	v_mfma_f32_16x16x32_f16 v[102:105], v[118:121], v[142:145], v[102:105]
	v_mfma_f32_16x16x32_f16 v[106:109], v[122:125], v[142:145], v[106:109]
	v_mfma_f32_16x16x32_f16 v[110:113], v[126:129], v[142:145], v[110:113]
	s_waitcnt lgkmcnt(0)
	v_mfma_f32_16x16x32_f16 v[114:117], v[114:117], v[146:149], v[2:5]
	v_mfma_f32_16x16x32_f16 v[118:121], v[118:121], v[146:149], v[6:9]
	v_mfma_f32_16x16x32_f16 v[122:125], v[122:125], v[146:149], v[10:13]
	v_mfma_f32_16x16x32_f16 v[126:129], v[126:129], v[146:149], v[14:17]
	s_setprio 1
	s_nop 1
	v_add_co_u32_e32 v14, vcc, s3, v166
	s_nop 1
	v_addc_co_u32_e32 v15, vcc, 0, v167, vcc
	global_load_dwordx4 v[2:5], v[14:15], off
	global_load_dwordx4 v[6:9], v[14:15], off offset:1024
	global_load_dwordx4 v[10:13], v[14:15], off offset:2048
	s_nop 0
	global_load_dwordx4 v[14:17], v[14:15], off offset:3072
	ds_read_b128 v[134:137], v132 offset:9216
	ds_read_b128 v[138:141], v132 offset:11264
	ds_read_b128 v[142:145], v132 offset:13312
	ds_read_b128 v[146:149], v132 offset:15360
	s_setprio 2
	s_waitcnt vmcnt(19) lgkmcnt(3)
	v_mfma_f32_16x16x32_f16 v[50:53], v[150:153], v[134:137], v[50:53]
	s_waitcnt vmcnt(18)
	v_mfma_f32_16x16x32_f16 v[70:73], v[154:157], v[134:137], v[70:73]
	s_waitcnt vmcnt(17)
	v_mfma_f32_16x16x32_f16 v[74:77], v[158:161], v[134:137], v[74:77]
	s_waitcnt vmcnt(16)
	v_mfma_f32_16x16x32_f16 v[78:81], v[162:165], v[134:137], v[78:81]
	s_waitcnt lgkmcnt(2)
	v_mfma_f32_16x16x32_f16 v[82:85], v[150:153], v[138:141], v[82:85]
	v_mfma_f32_16x16x32_f16 v[86:89], v[154:157], v[138:141], v[86:89]
	v_mfma_f32_16x16x32_f16 v[90:93], v[158:161], v[138:141], v[90:93]
	v_mfma_f32_16x16x32_f16 v[94:97], v[162:165], v[138:141], v[94:97]
	s_waitcnt lgkmcnt(1)
	v_mfma_f32_16x16x32_f16 v[98:101], v[150:153], v[142:145], v[98:101]
	v_mfma_f32_16x16x32_f16 v[102:105], v[154:157], v[142:145], v[102:105]
	v_mfma_f32_16x16x32_f16 v[106:109], v[158:161], v[142:145], v[106:109]
	v_mfma_f32_16x16x32_f16 v[110:113], v[162:165], v[142:145], v[110:113]
	s_waitcnt lgkmcnt(0)
	v_mfma_f32_16x16x32_f16 v[114:117], v[150:153], v[146:149], v[114:117]
	v_mfma_f32_16x16x32_f16 v[118:121], v[154:157], v[146:149], v[118:121]
	v_mfma_f32_16x16x32_f16 v[122:125], v[158:161], v[146:149], v[122:125]
	v_mfma_f32_16x16x32_f16 v[126:129], v[162:165], v[146:149], v[126:129]
	s_setprio 1
	s_add_i32 s5, s5, 6
	s_addk_i32 s4, 0x6000
	s_cmp_gt_u32 s5, 23
	s_cbranch_scc0 .LBB0_2
	v_lshrrev_b32_e32 v166, 2, v0
	v_and_b32_e32 v166, 12, v166
	v_and_b32_e32 v167, 0x1c0, v0
	v_or_b32_e32 v166, v167, v166
	v_lshlrev_b32_e32 v166, 2, v166
	global_load_dwordx4 v[150:153], v166, s[6:7]
	global_load_dwordx4 v[154:157], v166, s[6:7] offset:64
	global_load_dwordx4 v[158:161], v166, s[6:7] offset:128
	global_load_dwordx4 v[162:165], v166, s[6:7] offset:192
	s_waitcnt lgkmcnt(0)
	s_barrier
	ds_read_b128 v[134:137], v132
	ds_read_b128 v[138:141], v132 offset:2048
	ds_read_b128 v[142:145], v132 offset:4096
	ds_read_b128 v[146:149], v132 offset:6144
	s_setprio 2
	s_waitcnt vmcnt(19) lgkmcnt(3)
	v_mfma_f32_16x16x32_f16 v[50:53], v[54:57], v[134:137], v[50:53]
	s_waitcnt vmcnt(18)
	v_mfma_f32_16x16x32_f16 v[70:73], v[58:61], v[134:137], v[70:73]
	s_waitcnt vmcnt(17)
	v_mfma_f32_16x16x32_f16 v[74:77], v[62:65], v[134:137], v[74:77]
	s_waitcnt lgkmcnt(2)
	v_mfma_f32_16x16x32_f16 v[82:85], v[54:57], v[138:141], v[82:85]
	v_mfma_f32_16x16x32_f16 v[86:89], v[58:61], v[138:141], v[86:89]
	v_mfma_f32_16x16x32_f16 v[90:93], v[62:65], v[138:141], v[90:93]
	s_waitcnt lgkmcnt(1)
	v_mfma_f32_16x16x32_f16 v[98:101], v[54:57], v[142:145], v[98:101]
	v_mfma_f32_16x16x32_f16 v[102:105], v[58:61], v[142:145], v[102:105]
	v_mfma_f32_16x16x32_f16 v[106:109], v[62:65], v[142:145], v[106:109]
	s_waitcnt lgkmcnt(0)
	v_mfma_f32_16x16x32_f16 v[54:57], v[54:57], v[146:149], v[114:117]
	v_mfma_f32_16x16x32_f16 v[58:61], v[58:61], v[146:149], v[118:121]
	v_mfma_f32_16x16x32_f16 v[62:65], v[62:65], v[146:149], v[122:125]
	s_waitcnt vmcnt(16)
	v_mfma_f32_16x16x32_f16 v[78:81], v[66:69], v[134:137], v[78:81]
	v_mfma_f32_16x16x32_f16 v[94:97], v[66:69], v[138:141], v[94:97]
	v_mfma_f32_16x16x32_f16 v[110:113], v[66:69], v[142:145], v[110:113]
	v_mfma_f32_16x16x32_f16 v[66:69], v[66:69], v[146:149], v[126:129]
	s_setprio 1
	ds_read_b128 v[114:117], v132 offset:1024
	ds_read_b128 v[118:121], v132 offset:3072
	ds_read_b128 v[122:125], v132 offset:5120
	ds_read_b128 v[126:129], v132 offset:7168
	s_setprio 2
	s_waitcnt vmcnt(15) lgkmcnt(3)
	v_mfma_f32_16x16x32_f16 v[50:53], v[34:37], v[114:117], v[50:53]
	s_waitcnt vmcnt(14)
	v_mfma_f32_16x16x32_f16 v[70:73], v[38:41], v[114:117], v[70:73]
	s_waitcnt vmcnt(13)
	v_mfma_f32_16x16x32_f16 v[74:77], v[42:45], v[114:117], v[74:77]
	s_waitcnt vmcnt(12)
	v_mfma_f32_16x16x32_f16 v[78:81], v[46:49], v[114:117], v[78:81]
	s_waitcnt lgkmcnt(2)
	v_mfma_f32_16x16x32_f16 v[82:85], v[34:37], v[118:121], v[82:85]
	v_mfma_f32_16x16x32_f16 v[86:89], v[38:41], v[118:121], v[86:89]
	v_mfma_f32_16x16x32_f16 v[90:93], v[42:45], v[118:121], v[90:93]
	v_mfma_f32_16x16x32_f16 v[94:97], v[46:49], v[118:121], v[94:97]
	s_waitcnt lgkmcnt(1)
	v_mfma_f32_16x16x32_f16 v[98:101], v[34:37], v[122:125], v[98:101]
	v_mfma_f32_16x16x32_f16 v[102:105], v[38:41], v[122:125], v[102:105]
	v_mfma_f32_16x16x32_f16 v[106:109], v[42:45], v[122:125], v[106:109]
	v_mfma_f32_16x16x32_f16 v[110:113], v[46:49], v[122:125], v[110:113]
	s_waitcnt lgkmcnt(0)
	v_mfma_f32_16x16x32_f16 v[34:37], v[34:37], v[126:129], v[54:57]
	v_mfma_f32_16x16x32_f16 v[38:41], v[38:41], v[126:129], v[58:61]
	v_mfma_f32_16x16x32_f16 v[42:45], v[42:45], v[126:129], v[62:65]
	v_mfma_f32_16x16x32_f16 v[46:49], v[46:49], v[126:129], v[66:69]
	s_setprio 1
	s_waitcnt lgkmcnt(0)
	s_barrier
	ds_read_b128 v[54:57], v132 offset:8192
	ds_read_b128 v[58:61], v132 offset:10240
	ds_read_b128 v[62:65], v132 offset:12288
	ds_read_b128 v[66:69], v132 offset:14336
	s_setprio 2
	s_waitcnt vmcnt(11) lgkmcnt(3)
	v_mfma_f32_16x16x32_f16 v[50:53], v[30:33], v[54:57], v[50:53]
	s_waitcnt lgkmcnt(2)
	v_mfma_f32_16x16x32_f16 v[82:85], v[30:33], v[58:61], v[82:85]
	s_waitcnt vmcnt(10)
	v_mfma_f32_16x16x32_f16 v[86:89], v[18:21], v[58:61], v[86:89]
	s_waitcnt vmcnt(9)
	v_mfma_f32_16x16x32_f16 v[90:93], v[22:25], v[58:61], v[90:93]
	s_waitcnt vmcnt(8)
	v_mfma_f32_16x16x32_f16 v[58:61], v[26:29], v[58:61], v[94:97]
	s_waitcnt lgkmcnt(1)
	v_mfma_f32_16x16x32_f16 v[94:97], v[30:33], v[62:65], v[98:101]
	v_mfma_f32_16x16x32_f16 v[98:101], v[18:21], v[62:65], v[102:105]
	v_mfma_f32_16x16x32_f16 v[102:105], v[22:25], v[62:65], v[106:109]
	v_mfma_f32_16x16x32_f16 v[62:65], v[26:29], v[62:65], v[110:113]
	v_mfma_f32_16x16x32_f16 v[70:73], v[18:21], v[54:57], v[70:73]
	v_mfma_f32_16x16x32_f16 v[74:77], v[22:25], v[54:57], v[74:77]
	v_mfma_f32_16x16x32_f16 v[78:81], v[26:29], v[54:57], v[78:81]
	s_waitcnt lgkmcnt(0)
	v_mfma_f32_16x16x32_f16 v[106:109], v[30:33], v[66:69], v[34:37]
	v_mfma_f32_16x16x32_f16 v[110:113], v[18:21], v[66:69], v[38:41]
	v_mfma_f32_16x16x32_f16 v[114:117], v[22:25], v[66:69], v[42:45]
	v_mfma_f32_16x16x32_f16 v[66:69], v[26:29], v[66:69], v[46:49]
	s_setprio 1
	ds_read_b128 v[18:21], v132 offset:9216
	ds_read_b128 v[22:25], v132 offset:11264
	ds_read_b128 v[42:45], v132 offset:13312
	ds_read_b128 v[118:121], v132 offset:15360
	s_setprio 2
	s_waitcnt vmcnt(7) lgkmcnt(3)
	v_mfma_f32_16x16x32_f16 v[122:125], v[2:5], v[18:21], v[50:53]
	s_waitcnt vmcnt(6)
	v_mfma_f32_16x16x32_f16 v[54:57], v[6:9], v[18:21], v[70:73]
	s_waitcnt vmcnt(5)
	v_mfma_f32_16x16x32_f16 v[38:41], v[10:13], v[18:21], v[74:77]
	s_waitcnt vmcnt(4)
	v_mfma_f32_16x16x32_f16 v[26:29], v[14:17], v[18:21], v[78:81]
	s_waitcnt lgkmcnt(2)
	v_mfma_f32_16x16x32_f16 v[70:73], v[2:5], v[22:25], v[82:85]
	v_mfma_f32_16x16x32_f16 v[50:53], v[6:9], v[22:25], v[86:89]
	v_mfma_f32_16x16x32_f16 v[34:37], v[10:13], v[22:25], v[90:93]
	v_mfma_f32_16x16x32_f16 v[22:25], v[14:17], v[22:25], v[58:61]
	s_waitcnt lgkmcnt(1)
	v_mfma_f32_16x16x32_f16 v[74:77], v[2:5], v[42:45], v[94:97]
	v_mfma_f32_16x16x32_f16 v[46:49], v[6:9], v[42:45], v[98:101]
	v_mfma_f32_16x16x32_f16 v[30:33], v[10:13], v[42:45], v[102:105]
	v_mfma_f32_16x16x32_f16 v[18:21], v[14:17], v[42:45], v[62:65]
	s_waitcnt lgkmcnt(0)
	v_mfma_f32_16x16x32_f16 v[62:65], v[2:5], v[118:121], v[106:109]
	v_mfma_f32_16x16x32_f16 v[42:45], v[6:9], v[118:121], v[110:113]
	v_mfma_f32_16x16x32_f16 v[6:9], v[10:13], v[118:121], v[114:117]
	v_mfma_f32_16x16x32_f16 v[2:5], v[14:17], v[118:121], v[66:69]
	s_setprio 1
	v_lshrrev_b32_e32 v10, 2, v0
	v_and_b32_e32 v10, 12, v10
	s_movk_i32 s3, 0x1c0
	v_and_or_b32 v0, v0, s3, v10
	v_lshlrev_b32_e32 v0, 2, v0
	s_waitcnt vmcnt(0)
	v_mov_b32_e32 v10, v150
	v_mov_b32_e32 v11, v151
	v_mov_b32_e32 v12, v152
	v_mov_b32_e32 v13, v153
	v_mbcnt_lo_u32_b32 v14, -1, 0
	v_cmp_eq_u32_e32 vcc, 0, v1
	v_mbcnt_hi_u32_b32 v1, -1, v14
	v_and_b32_e32 v15, 64, v1
	v_xor_b32_e32 v14, 1, v1
	v_add_u32_e32 v78, 64, v15
	v_cmp_lt_i32_e64 s[4:5], v14, v78
	v_xor_b32_e32 v61, 2, v1
	v_xor_b32_e32 v68, 4, v1
	v_cndmask_b32_e64 v14, v1, v14, s[4:5]
	v_lshlrev_b32_e32 v60, 2, v14
	v_cmp_lt_i32_e64 s[4:5], v61, v78
	v_xor_b32_e32 v69, 8, v1
	s_ashr_i32 s3, s2, 31
	s_lshl_b64 s[12:13], s[2:3], 11
	s_waitcnt vmcnt(0)
	v_fmamk_f32 v14, v122, 0x3c800000, v10
	v_fmamk_f32 v15, v123, 0x3c800000, v11
	v_fmamk_f32 v16, v124, 0x3c800000, v12
	v_fmamk_f32 v17, v125, 0x3c800000, v13
	v_fmamk_f32 v58, v70, 0x3c800000, v10
	v_fmamk_f32 v59, v71, 0x3c800000, v11
	v_fmamk_f32 v66, v72, 0x3c800000, v12
	v_fmamk_f32 v67, v73, 0x3c800000, v13
	v_fmamk_f32 v70, v74, 0x3c800000, v10
	v_fmamk_f32 v71, v75, 0x3c800000, v11
	v_fmamk_f32 v74, v62, 0x3c800000, v10
	v_fmamk_f32 v75, v63, 0x3c800000, v11
	v_max_f32_e32 v10, 0, v14
	v_max_f32_e32 v11, 0, v15
	v_max_f32_e32 v14, 0, v16
	v_max_f32_e32 v15, 0, v17
	v_fmamk_f32 v72, v76, 0x3c800000, v12
	v_fmamk_f32 v73, v77, 0x3c800000, v13
	v_max_f32_e32 v16, 0, v58
	v_max_f32_e32 v17, 0, v59
	v_max_f32_e32 v58, 0, v66
	v_max_f32_e32 v59, 0, v67
	v_pk_add_f32 v[10:11], v[10:11], 0 op_sel_hi:[1,0]
	v_pk_add_f32 v[14:15], v[14:15], 0 op_sel_hi:[1,0]
	v_fmamk_f32 v12, v64, 0x3c800000, v12
	v_fmac_f32_e32 v13, 0x3c800000, v65
	v_max_f32_e32 v62, 0, v70
	v_max_f32_e32 v63, 0, v71
	v_max_f32_e32 v64, 0, v72
	v_max_f32_e32 v65, 0, v73
	v_pk_add_f32 v[10:11], v[10:11], v[16:17]
	v_pk_add_f32 v[14:15], v[14:15], v[58:59]
	v_max_f32_e32 v66, 0, v74
	v_max_f32_e32 v67, 0, v75
	v_max_f32_e32 v12, 0, v12
	v_max_f32_e32 v13, 0, v13
	v_pk_add_f32 v[10:11], v[10:11], v[62:63]
	v_pk_add_f32 v[14:15], v[14:15], v[64:65]
	v_pk_add_f32 v[10:11], v[10:11], v[66:67]
	v_pk_add_f32 v[12:13], v[14:15], v[12:13]
	ds_bpermute_b32 v14, v60, v10
	ds_bpermute_b32 v15, v60, v11
	ds_bpermute_b32 v16, v60, v12
	ds_bpermute_b32 v17, v60, v13
	v_cndmask_b32_e64 v58, v1, v61, s[4:5]
	v_lshlrev_b32_e32 v61, 2, v58
	s_waitcnt lgkmcnt(2)
	v_pk_add_f32 v[10:11], v[10:11], v[14:15]
	ds_bpermute_b32 v14, v61, v10
	s_waitcnt lgkmcnt(1)
	v_pk_add_f32 v[12:13], v[12:13], v[16:17]
	ds_bpermute_b32 v15, v61, v11
	ds_bpermute_b32 v16, v61, v12
	ds_bpermute_b32 v17, v61, v13
	v_cmp_lt_i32_e64 s[4:5], v68, v78
	s_waitcnt lgkmcnt(2)
	v_pk_add_f32 v[10:11], v[10:11], v[14:15]
	v_cndmask_b32_e64 v58, v1, v68, s[4:5]
	v_lshlrev_b32_e32 v62, 2, v58
	s_waitcnt lgkmcnt(0)
	v_pk_add_f32 v[14:15], v[12:13], v[16:17]
	ds_bpermute_b32 v12, v62, v10
	ds_bpermute_b32 v13, v62, v11
	ds_bpermute_b32 v16, v62, v14
	ds_bpermute_b32 v17, v62, v15
	v_cmp_lt_i32_e64 s[4:5], v69, v78
	s_waitcnt lgkmcnt(2)
	v_pk_add_f32 v[12:13], v[10:11], v[12:13]
	v_cndmask_b32_e64 v1, v1, v69, s[4:5]
	v_lshlrev_b32_e32 v63, 2, v1
	s_waitcnt lgkmcnt(0)
	v_pk_add_f32 v[16:17], v[14:15], v[16:17]
	ds_bpermute_b32 v14, v63, v12
	ds_bpermute_b32 v15, v63, v13
	ds_bpermute_b32 v58, v63, v16
	ds_bpermute_b32 v59, v63, v17
	s_add_u32 s4, s10, s12
	v_mov_b32_e32 v1, 0
	s_addc_u32 s5, s11, s13
	v_lshl_add_u64 v[10:11], s[6:7], 0, v[0:1]
	s_and_saveexec_b64 s[6:7], vcc
	s_cbranch_execz .LBB0_5
	s_waitcnt lgkmcnt(0)
	v_pk_add_f32 v[16:17], v[16:17], v[58:59]
	v_pk_add_f32 v[14:15], v[12:13], v[14:15]
	global_store_dwordx4 v0, v[14:17], s[4:5]
.LBB0_5:
	s_or_b64 exec, exec, s[6:7]
	s_waitcnt lgkmcnt(2)
	v_mov_b32_e32 v12, v154
	v_mov_b32_e32 v13, v155
	v_mov_b32_e32 v14, v156
	v_mov_b32_e32 v15, v157
	s_waitcnt vmcnt(0)
	v_fmamk_f32 v1, v54, 0x3c800000, v12
	v_fmamk_f32 v16, v55, 0x3c800000, v13
	v_fmamk_f32 v17, v56, 0x3c800000, v14
	v_fmamk_f32 v54, v57, 0x3c800000, v15
	v_fmamk_f32 v50, v50, 0x3c800000, v12
	v_fmamk_f32 v51, v51, 0x3c800000, v13
	v_fmamk_f32 v52, v52, 0x3c800000, v14
	v_fmamk_f32 v53, v53, 0x3c800000, v15
	v_fmamk_f32 v46, v46, 0x3c800000, v12
	v_fmamk_f32 v47, v47, 0x3c800000, v13
	v_fmamk_f32 v55, v42, 0x3c800000, v12
	v_fmamk_f32 v56, v43, 0x3c800000, v13
	v_max_f32_e32 v12, 0, v1
	v_max_f32_e32 v13, 0, v16
	v_max_f32_e32 v16, 0, v17
	v_max_f32_e32 v17, 0, v54
	v_fmamk_f32 v48, v48, 0x3c800000, v14
	v_fmamk_f32 v49, v49, 0x3c800000, v15
	v_fmamk_f32 v14, v44, 0x3c800000, v14
	v_fmac_f32_e32 v15, 0x3c800000, v45
	v_max_f32_e32 v42, 0, v50
	v_max_f32_e32 v43, 0, v51
	v_max_f32_e32 v44, 0, v52
	v_max_f32_e32 v45, 0, v53
	v_pk_add_f32 v[12:13], v[12:13], 0 op_sel_hi:[1,0]
	v_pk_add_f32 v[16:17], v[16:17], 0 op_sel_hi:[1,0]
	v_max_f32_e32 v46, 0, v46
	v_max_f32_e32 v47, 0, v47
	v_max_f32_e32 v48, 0, v48
	v_max_f32_e32 v49, 0, v49
	v_pk_add_f32 v[12:13], v[12:13], v[42:43]
	v_pk_add_f32 v[16:17], v[16:17], v[44:45]
	v_max_f32_e32 v50, 0, v55
	v_max_f32_e32 v51, 0, v56
	v_max_f32_e32 v14, 0, v14
	v_max_f32_e32 v15, 0, v15
	v_pk_add_f32 v[12:13], v[12:13], v[46:47]
	v_pk_add_f32 v[16:17], v[16:17], v[48:49]
	v_pk_add_f32 v[12:13], v[12:13], v[50:51]
	v_pk_add_f32 v[14:15], v[16:17], v[14:15]
	ds_bpermute_b32 v16, v60, v12
	ds_bpermute_b32 v17, v60, v13
	ds_bpermute_b32 v42, v60, v14
	ds_bpermute_b32 v43, v60, v15
	s_waitcnt lgkmcnt(2)
	v_pk_add_f32 v[12:13], v[12:13], v[16:17]
	ds_bpermute_b32 v16, v61, v12
	s_waitcnt lgkmcnt(1)
	v_pk_add_f32 v[14:15], v[14:15], v[42:43]
	ds_bpermute_b32 v17, v61, v13
	ds_bpermute_b32 v42, v61, v14
	ds_bpermute_b32 v43, v61, v15
	s_waitcnt lgkmcnt(2)
	v_pk_add_f32 v[12:13], v[12:13], v[16:17]
	ds_bpermute_b32 v16, v62, v12
	s_waitcnt lgkmcnt(1)
	v_pk_add_f32 v[14:15], v[14:15], v[42:43]
	ds_bpermute_b32 v17, v62, v13
	ds_bpermute_b32 v42, v62, v14
	ds_bpermute_b32 v43, v62, v15
	s_waitcnt lgkmcnt(2)
	v_pk_add_f32 v[12:13], v[12:13], v[16:17]
	s_waitcnt lgkmcnt(0)
	v_pk_add_f32 v[16:17], v[14:15], v[42:43]
	ds_bpermute_b32 v14, v63, v12
	ds_bpermute_b32 v15, v63, v13
	ds_bpermute_b32 v42, v63, v16
	ds_bpermute_b32 v43, v63, v17
	s_and_saveexec_b64 s[6:7], vcc
	s_cbranch_execz .LBB0_7
	s_waitcnt lgkmcnt(0)
	v_pk_add_f32 v[16:17], v[16:17], v[42:43]
	v_pk_add_f32 v[14:15], v[12:13], v[14:15]
	global_store_dwordx4 v0, v[14:17], s[4:5] offset:64
.LBB0_7:
	s_or_b64 exec, exec, s[6:7]
	s_waitcnt lgkmcnt(2)
	v_mov_b32_e32 v12, v158
	v_mov_b32_e32 v13, v159
	v_mov_b32_e32 v14, v160
	v_mov_b32_e32 v15, v161
	s_waitcnt vmcnt(0)
	v_fmamk_f32 v1, v38, 0x3c800000, v12
	v_fmamk_f32 v16, v39, 0x3c800000, v13
	v_fmamk_f32 v17, v40, 0x3c800000, v14
	v_fmamk_f32 v38, v41, 0x3c800000, v15
	v_fmamk_f32 v34, v34, 0x3c800000, v12
	v_fmamk_f32 v35, v35, 0x3c800000, v13
	v_fmamk_f32 v36, v36, 0x3c800000, v14
	v_fmamk_f32 v37, v37, 0x3c800000, v15
	v_fmamk_f32 v32, v32, 0x3c800000, v14
	v_fmamk_f32 v33, v33, 0x3c800000, v15
	v_fmamk_f32 v39, v6, 0x3c800000, v12
	v_fmamk_f32 v40, v7, 0x3c800000, v13
	v_fmamk_f32 v14, v8, 0x3c800000, v14
	v_fmac_f32_e32 v15, 0x3c800000, v9
	v_max_f32_e32 v6, 0, v1
	v_max_f32_e32 v7, 0, v16
	v_max_f32_e32 v8, 0, v17
	v_max_f32_e32 v9, 0, v38
	v_fmamk_f32 v30, v30, 0x3c800000, v12
	v_fmamk_f32 v31, v31, 0x3c800000, v13
	v_max_f32_e32 v12, 0, v34
	v_max_f32_e32 v13, 0, v35
	v_max_f32_e32 v16, 0, v36
	v_max_f32_e32 v17, 0, v37
	v_pk_add_f32 v[6:7], v[6:7], 0 op_sel_hi:[1,0]
	v_pk_add_f32 v[8:9], v[8:9], 0 op_sel_hi:[1,0]
	v_max_f32_e32 v30, 0, v30
	v_max_f32_e32 v31, 0, v31
	v_max_f32_e32 v32, 0, v32
	v_max_f32_e32 v33, 0, v33
	v_pk_add_f32 v[6:7], v[6:7], v[12:13]
	v_pk_add_f32 v[8:9], v[8:9], v[16:17]
	v_max_f32_e32 v34, 0, v39
	v_max_f32_e32 v35, 0, v40
	v_max_f32_e32 v14, 0, v14
	v_max_f32_e32 v15, 0, v15
	v_pk_add_f32 v[6:7], v[6:7], v[30:31]
	v_pk_add_f32 v[8:9], v[8:9], v[32:33]
	v_pk_add_f32 v[6:7], v[6:7], v[34:35]
	v_pk_add_f32 v[8:9], v[8:9], v[14:15]
	ds_bpermute_b32 v12, v60, v6
	ds_bpermute_b32 v13, v60, v7
	ds_bpermute_b32 v14, v60, v8
	ds_bpermute_b32 v15, v60, v9
	s_waitcnt lgkmcnt(2)
	v_pk_add_f32 v[6:7], v[6:7], v[12:13]
	ds_bpermute_b32 v12, v61, v6
	s_waitcnt lgkmcnt(1)
	v_pk_add_f32 v[8:9], v[8:9], v[14:15]
	ds_bpermute_b32 v13, v61, v7
	ds_bpermute_b32 v14, v61, v8
	ds_bpermute_b32 v15, v61, v9
	s_waitcnt lgkmcnt(2)
	v_pk_add_f32 v[6:7], v[6:7], v[12:13]
	ds_bpermute_b32 v12, v62, v6
	s_waitcnt lgkmcnt(1)
	v_pk_add_f32 v[8:9], v[8:9], v[14:15]
	ds_bpermute_b32 v13, v62, v7
	ds_bpermute_b32 v14, v62, v8
	ds_bpermute_b32 v15, v62, v9
	s_waitcnt lgkmcnt(2)
	v_pk_add_f32 v[6:7], v[6:7], v[12:13]
	s_waitcnt lgkmcnt(0)
	v_pk_add_f32 v[12:13], v[8:9], v[14:15]
	ds_bpermute_b32 v8, v63, v6
	ds_bpermute_b32 v9, v63, v7
	ds_bpermute_b32 v14, v63, v12
	ds_bpermute_b32 v15, v63, v13
	s_and_saveexec_b64 s[6:7], vcc
	s_cbranch_execz .LBB0_9
	s_waitcnt lgkmcnt(0)
	v_pk_add_f32 v[14:15], v[12:13], v[14:15]
	v_pk_add_f32 v[12:13], v[6:7], v[8:9]
	global_store_dwordx4 v0, v[12:15], s[4:5] offset:128
.LBB0_9:
	s_or_b64 exec, exec, s[6:7]
	s_waitcnt lgkmcnt(2)
	v_mov_b32_e32 v6, v162
	v_mov_b32_e32 v7, v163
	v_mov_b32_e32 v8, v164
	v_mov_b32_e32 v9, v165
	s_waitcnt vmcnt(0)
	v_fmamk_f32 v1, v26, 0x3c800000, v6
	v_fmamk_f32 v10, v27, 0x3c800000, v7
	v_fmamk_f32 v11, v28, 0x3c800000, v8
	v_fmamk_f32 v12, v29, 0x3c800000, v9
	v_fmamk_f32 v13, v22, 0x3c800000, v6
	s_waitcnt lgkmcnt(1)
	v_fmamk_f32 v14, v23, 0x3c800000, v7
	s_waitcnt lgkmcnt(0)
	v_fmamk_f32 v15, v24, 0x3c800000, v8
	v_fmamk_f32 v16, v25, 0x3c800000, v9
	v_fmamk_f32 v17, v18, 0x3c800000, v6
	v_fmamk_f32 v18, v19, 0x3c800000, v7
	v_fmamk_f32 v19, v20, 0x3c800000, v8
	v_fmamk_f32 v20, v21, 0x3c800000, v9
	v_fmamk_f32 v21, v2, 0x3c800000, v6
	v_fmamk_f32 v22, v3, 0x3c800000, v7
	v_fmamk_f32 v8, v4, 0x3c800000, v8
	v_fmac_f32_e32 v9, 0x3c800000, v5
	v_max_f32_e32 v2, 0, v1
	v_max_f32_e32 v3, 0, v10
	v_max_f32_e32 v4, 0, v11
	v_max_f32_e32 v5, 0, v12
	v_max_f32_e32 v6, 0, v13
	v_max_f32_e32 v7, 0, v14
	v_max_f32_e32 v10, 0, v15
	v_max_f32_e32 v11, 0, v16
	v_pk_add_f32 v[2:3], v[2:3], 0 op_sel_hi:[1,0]
	v_pk_add_f32 v[4:5], v[4:5], 0 op_sel_hi:[1,0]
	v_max_f32_e32 v12, 0, v17
	v_max_f32_e32 v13, 0, v18
	v_max_f32_e32 v14, 0, v19
	v_max_f32_e32 v15, 0, v20
	v_pk_add_f32 v[2:3], v[2:3], v[6:7]
	v_pk_add_f32 v[4:5], v[4:5], v[10:11]
	v_max_f32_e32 v16, 0, v21
	v_max_f32_e32 v17, 0, v22
	v_max_f32_e32 v8, 0, v8
	v_max_f32_e32 v9, 0, v9
	v_pk_add_f32 v[2:3], v[2:3], v[12:13]
	v_pk_add_f32 v[4:5], v[4:5], v[14:15]
	v_pk_add_f32 v[2:3], v[2:3], v[16:17]
	v_pk_add_f32 v[4:5], v[4:5], v[8:9]
	ds_bpermute_b32 v6, v60, v2
	ds_bpermute_b32 v7, v60, v3
	ds_bpermute_b32 v8, v60, v4
	ds_bpermute_b32 v9, v60, v5
	s_waitcnt lgkmcnt(2)
	v_pk_add_f32 v[2:3], v[2:3], v[6:7]
	ds_bpermute_b32 v6, v61, v2
	s_waitcnt lgkmcnt(1)
	v_pk_add_f32 v[4:5], v[4:5], v[8:9]
	ds_bpermute_b32 v7, v61, v3
	ds_bpermute_b32 v8, v61, v4
	ds_bpermute_b32 v9, v61, v5
	s_waitcnt lgkmcnt(2)
	v_pk_add_f32 v[2:3], v[2:3], v[6:7]
	ds_bpermute_b32 v6, v62, v2
	s_waitcnt lgkmcnt(1)
	v_pk_add_f32 v[4:5], v[4:5], v[8:9]
	ds_bpermute_b32 v7, v62, v3
	ds_bpermute_b32 v8, v62, v4
	ds_bpermute_b32 v9, v62, v5
	s_waitcnt lgkmcnt(2)
	v_pk_add_f32 v[2:3], v[2:3], v[6:7]
	s_waitcnt lgkmcnt(0)
	v_pk_add_f32 v[6:7], v[4:5], v[8:9]
	ds_bpermute_b32 v4, v63, v2
	ds_bpermute_b32 v5, v63, v3
	ds_bpermute_b32 v8, v63, v6
	ds_bpermute_b32 v9, v63, v7
	s_and_saveexec_b64 s[6:7], vcc
	s_cbranch_execz .LBB0_11
	s_waitcnt lgkmcnt(0)
	v_pk_add_f32 v[6:7], v[6:7], v[8:9]
	v_pk_add_f32 v[4:5], v[2:3], v[4:5]
	global_store_dwordx4 v0, v[4:7], s[4:5] offset:192
